# s17_swp
# speedup vs baseline: 1.0783x; 1.0127x over previous
.LBB2_3:
	s_load_dwordx8 s[12:19], s[0:1], 0x10
	v_lshrrev_b32_e32 v2, 2, v0
	s_lshr_b32 s5, s21, 8
	v_sub_u32_e32 v2, 0, v2
	v_and_b32_e32 v102, 15, v0
	v_bitop3_b32 v2, v120, v2, 3 bitop3:0x78
	s_mul_i32 s25, s5, 0x60
	s_and_b32 s2, s22, 3
	v_lshlrev_b32_e32 v98, 4, v2
	v_or_b32_e32 v2, s25, v102
	v_mov_b32_e32 v50, 0
	s_mov_b32 s3, 0
	v_lshlrev_b32_e32 v99, 6, v2
	s_lshl_b32 s6, s2, 12
	s_mov_b32 s7, 32
	v_mov_b32_e32 v51, v50
	v_mov_b32_e32 v52, v50
	v_mov_b32_e32 v53, v50
	v_mov_b32_e32 v74, v50
	v_mov_b32_e32 v75, v50
	v_mov_b32_e32 v76, v50
	v_mov_b32_e32 v77, v50
	v_mov_b32_e32 v6, v50
	v_mov_b32_e32 v7, v50
	v_mov_b32_e32 v8, v50
	v_mov_b32_e32 v9, v50
	v_mov_b32_e32 v26, v50
	v_mov_b32_e32 v27, v50
	v_mov_b32_e32 v28, v50
	v_mov_b32_e32 v29, v50
	v_mov_b32_e32 v54, v50
	v_mov_b32_e32 v55, v50
	v_mov_b32_e32 v56, v50
	v_mov_b32_e32 v57, v50
	v_mov_b32_e32 v86, v50
	v_mov_b32_e32 v87, v50
	v_mov_b32_e32 v88, v50
	v_mov_b32_e32 v89, v50
	v_mov_b32_e32 v18, v50
	v_mov_b32_e32 v19, v50
	v_mov_b32_e32 v20, v50
	v_mov_b32_e32 v21, v50
	v_mov_b32_e32 v42, v50
	v_mov_b32_e32 v43, v50
	v_mov_b32_e32 v44, v50
	v_mov_b32_e32 v45, v50
	v_mov_b32_e32 v66, v50
	v_mov_b32_e32 v67, v50
	v_mov_b32_e32 v68, v50
	v_mov_b32_e32 v69, v50
	v_mov_b32_e32 v90, v50
	v_mov_b32_e32 v91, v50
	v_mov_b32_e32 v92, v50
	v_mov_b32_e32 v93, v50
	v_mov_b32_e32 v22, v50
	v_mov_b32_e32 v23, v50
	v_mov_b32_e32 v24, v50
	v_mov_b32_e32 v25, v50
	v_mov_b32_e32 v46, v50
	v_mov_b32_e32 v47, v50
	v_mov_b32_e32 v48, v50
	v_mov_b32_e32 v49, v50
	v_mov_b32_e32 v70, v50
	v_mov_b32_e32 v71, v50
	v_mov_b32_e32 v72, v50
	v_mov_b32_e32 v73, v50
	v_mov_b32_e32 v94, v50
	v_mov_b32_e32 v95, v50
	v_mov_b32_e32 v96, v50
	v_mov_b32_e32 v97, v50
	v_mov_b32_e32 v38, v50
	v_mov_b32_e32 v39, v50
	v_mov_b32_e32 v40, v50
	v_mov_b32_e32 v41, v50
	v_mov_b32_e32 v14, v50
	v_mov_b32_e32 v15, v50
	v_mov_b32_e32 v16, v50
	v_mov_b32_e32 v17, v50
	v_mov_b32_e32 v82, v50
	v_mov_b32_e32 v83, v50
	v_mov_b32_e32 v84, v50
	v_mov_b32_e32 v85, v50
	v_mov_b32_e32 v58, v50
	v_mov_b32_e32 v59, v50
	v_mov_b32_e32 v60, v50
	v_mov_b32_e32 v61, v50
	v_mov_b32_e32 v30, v50
	v_mov_b32_e32 v31, v50
	v_mov_b32_e32 v32, v50
	v_mov_b32_e32 v33, v50
	v_mov_b32_e32 v10, v50
	v_mov_b32_e32 v11, v50
	v_mov_b32_e32 v12, v50
	v_mov_b32_e32 v13, v50
	v_mov_b32_e32 v78, v50
	v_mov_b32_e32 v79, v50
	v_mov_b32_e32 v80, v50
	v_mov_b32_e32 v81, v50
	v_mov_b32_e32 v62, v50
	v_mov_b32_e32 v63, v50
	v_mov_b32_e32 v64, v50
	v_mov_b32_e32 v65, v50
	v_mov_b32_e32 v34, v50
	v_mov_b32_e32 v35, v50
	v_mov_b32_e32 v36, v50
	v_mov_b32_e32 v37, v50
	v_mov_b32_e32 v2, v50
	v_mov_b32_e32 v3, v50
	v_mov_b32_e32 v4, v50
	v_mov_b32_e32 v5, v50
	v_lshlrev_b32_e32 v100, 6, v102
	v_add_u32_e32 v99, v99, v98
	v_add3_u32 v100, s6, v100, v98
	s_barrier
	ds_read_b128 v[104:107], v100 offset:12288
	ds_read_b128 v[108:111], v100 offset:13312
	ds_read_b128 v[112:115], v100 offset:14336
	ds_read_b128 v[116:119], v100 offset:15360
	ds_read_b128 v[122:125], v99
	ds_read_b128 v[126:129], v99 offset:1024
	ds_read_b128 v[130:133], v99 offset:2048
	ds_read_b128 v[134:137], v99 offset:3072
	ds_read_b128 v[138:141], v99 offset:4096
	ds_read_b128 v[142:145], v99 offset:5120
	s_mov_b32 s3, 1
	s_mov_b32 s7, 16
.Lg0_cloop:
	s_mul_i32 s8, s3, 0x7000
	s_barrier
	v_add_u32_e32 v103, s8, v100
	v_add_u32_e32 v101, s8, v99
	ds_read_b128 v[146:149], v103 offset:12288
	ds_read_b128 v[150:153], v103 offset:13312
	ds_read_b128 v[154:157], v103 offset:14336
	ds_read_b128 v[158:161], v103 offset:15360
	s_waitcnt lgkmcnt(9)
	v_mfma_f32_16x16x32_f16 v[94:97], v[122:125], v[104:107], v[94:97]
	s_add_i32 s8, s3, 1
	s_cmp_lg_u32 s3, 4
	s_cselect_b32 s3, s8, 0
	v_mfma_f32_16x16x32_f16 v[70:73], v[122:125], v[108:111], v[70:73]
	v_mfma_f32_16x16x32_f16 v[46:49], v[122:125], v[112:115], v[46:49]
	v_mfma_f32_16x16x32_f16 v[22:25], v[122:125], v[116:119], v[22:25]
	ds_read_b128 v[122:125], v101
	s_waitcnt lgkmcnt(9)
	v_mfma_f32_16x16x32_f16 v[90:93], v[126:129], v[104:107], v[90:93]
	v_mfma_f32_16x16x32_f16 v[66:69], v[126:129], v[108:111], v[66:69]
	v_mfma_f32_16x16x32_f16 v[42:45], v[126:129], v[112:115], v[42:45]
	v_mfma_f32_16x16x32_f16 v[18:21], v[126:129], v[116:119], v[18:21]
	ds_read_b128 v[126:129], v101 offset:1024
	s_waitcnt lgkmcnt(9)
	v_mfma_f32_16x16x32_f16 v[86:89], v[130:133], v[104:107], v[86:89]
	v_mfma_f32_16x16x32_f16 v[54:57], v[130:133], v[108:111], v[54:57]
	v_mfma_f32_16x16x32_f16 v[26:29], v[130:133], v[112:115], v[26:29]
	v_mfma_f32_16x16x32_f16 v[6:9], v[130:133], v[116:119], v[6:9]
	ds_read_b128 v[130:133], v101 offset:2048
	s_waitcnt lgkmcnt(9)
	v_mfma_f32_16x16x32_f16 v[74:77], v[134:137], v[104:107], v[74:77]
	v_mfma_f32_16x16x32_f16 v[50:53], v[134:137], v[108:111], v[50:53]
	v_mfma_f32_16x16x32_f16 v[38:41], v[134:137], v[112:115], v[38:41]
	v_mfma_f32_16x16x32_f16 v[14:17], v[134:137], v[116:119], v[14:17]
	ds_read_b128 v[134:137], v101 offset:3072
	s_waitcnt lgkmcnt(9)
	v_mfma_f32_16x16x32_f16 v[82:85], v[138:141], v[104:107], v[82:85]
	v_mfma_f32_16x16x32_f16 v[58:61], v[138:141], v[108:111], v[58:61]
	v_mfma_f32_16x16x32_f16 v[30:33], v[138:141], v[112:115], v[30:33]
	v_mfma_f32_16x16x32_f16 v[10:13], v[138:141], v[116:119], v[10:13]
	ds_read_b128 v[138:141], v101 offset:4096
	s_waitcnt lgkmcnt(9)
	v_mfma_f32_16x16x32_f16 v[78:81], v[142:145], v[104:107], v[78:81]
	v_mfma_f32_16x16x32_f16 v[62:65], v[142:145], v[108:111], v[62:65]
	v_mfma_f32_16x16x32_f16 v[34:37], v[142:145], v[112:115], v[34:37]
	v_mfma_f32_16x16x32_f16 v[2:5], v[142:145], v[116:119], v[2:5]
	ds_read_b128 v[142:145], v101 offset:5120
	s_mul_i32 s8, s3, 0x7000
	s_barrier
	v_add_u32_e32 v103, s8, v100
	v_add_u32_e32 v101, s8, v99
	ds_read_b128 v[104:107], v103 offset:12288
	ds_read_b128 v[108:111], v103 offset:13312
	ds_read_b128 v[112:115], v103 offset:14336
	ds_read_b128 v[116:119], v103 offset:15360
	s_waitcnt lgkmcnt(9)
	v_mfma_f32_16x16x32_f16 v[94:97], v[122:125], v[146:149], v[94:97]
	s_add_i32 s8, s3, 1
	s_cmp_lg_u32 s3, 4
	s_cselect_b32 s3, s8, 0
	v_mfma_f32_16x16x32_f16 v[70:73], v[122:125], v[150:153], v[70:73]
	v_mfma_f32_16x16x32_f16 v[46:49], v[122:125], v[154:157], v[46:49]
	v_mfma_f32_16x16x32_f16 v[22:25], v[122:125], v[158:161], v[22:25]
	ds_read_b128 v[122:125], v101
	s_waitcnt lgkmcnt(9)
	v_mfma_f32_16x16x32_f16 v[90:93], v[126:129], v[146:149], v[90:93]
	v_mfma_f32_16x16x32_f16 v[66:69], v[126:129], v[150:153], v[66:69]
	v_mfma_f32_16x16x32_f16 v[42:45], v[126:129], v[154:157], v[42:45]
	v_mfma_f32_16x16x32_f16 v[18:21], v[126:129], v[158:161], v[18:21]
	ds_read_b128 v[126:129], v101 offset:1024
	s_waitcnt lgkmcnt(9)
	v_mfma_f32_16x16x32_f16 v[86:89], v[130:133], v[146:149], v[86:89]
	v_mfma_f32_16x16x32_f16 v[54:57], v[130:133], v[150:153], v[54:57]
	v_mfma_f32_16x16x32_f16 v[26:29], v[130:133], v[154:157], v[26:29]
	v_mfma_f32_16x16x32_f16 v[6:9], v[130:133], v[158:161], v[6:9]
	ds_read_b128 v[130:133], v101 offset:2048
	s_waitcnt lgkmcnt(9)
	v_mfma_f32_16x16x32_f16 v[74:77], v[134:137], v[146:149], v[74:77]
	v_mfma_f32_16x16x32_f16 v[50:53], v[134:137], v[150:153], v[50:53]
	v_mfma_f32_16x16x32_f16 v[38:41], v[134:137], v[154:157], v[38:41]
	v_mfma_f32_16x16x32_f16 v[14:17], v[134:137], v[158:161], v[14:17]
	ds_read_b128 v[134:137], v101 offset:3072
	s_waitcnt lgkmcnt(9)
	v_mfma_f32_16x16x32_f16 v[82:85], v[138:141], v[146:149], v[82:85]
	v_mfma_f32_16x16x32_f16 v[58:61], v[138:141], v[150:153], v[58:61]
	v_mfma_f32_16x16x32_f16 v[30:33], v[138:141], v[154:157], v[30:33]
	v_mfma_f32_16x16x32_f16 v[10:13], v[138:141], v[158:161], v[10:13]
	ds_read_b128 v[138:141], v101 offset:4096
	s_waitcnt lgkmcnt(9)
	v_mfma_f32_16x16x32_f16 v[78:81], v[142:145], v[146:149], v[78:81]
	v_mfma_f32_16x16x32_f16 v[62:65], v[142:145], v[150:153], v[62:65]
	v_mfma_f32_16x16x32_f16 v[34:37], v[142:145], v[154:157], v[34:37]
	v_mfma_f32_16x16x32_f16 v[2:5], v[142:145], v[158:161], v[2:5]
	ds_read_b128 v[142:145], v101 offset:5120
	s_add_i32 s7, s7, -1
	s_cmp_eq_u32 s7, 0
	s_cbranch_scc0 .Lg0_cloop
	s_waitcnt lgkmcnt(0)
	s_barrier
	s_mul_i32 s24, s22, 0x3400
	s_lshl_b32 s28, s2, 6
	s_add_i32 s29, s20, s28
	s_and_b32 s30, s29, 0x7ff
	v_add_u32_e32 v98, s30, v102
	v_lshlrev_b32_e32 v98, 8, v98
	v_lshl_add_u32 v98, v120, 4, v98
	v_add_u32_e32 v99, 0x1000, v98
	v_add_u32_e32 v100, 0x2000, v98
	v_add_u32_e32 v101, 0x3000, v98
	v_mul_u32_u24_e32 v103, 0xd0, v102
	v_lshl_add_u32 v103, v120, 3, v103
	v_add_u32_e32 v103, s24, v103
	v_lshrrev_b32_e32 v0, 2, v1
	v_and_b32_e32 v1, 3, v1
	v_mul_u32_u24_e32 v102, 0xd0, v0
	v_lshl_add_u32 v102, v1, 4, v102
	v_add_u32_e32 v102, s24, v102
	v_lshlrev_b32_e32 v0, 11, v0
	v_lshl_add_u32 v0, v1, 4, v0
	s_lshl_b32 s31, s5, 7
	s_add_i32 s35, s31, 0
	s_and_b32 s35, s35, 0xff
	s_add_u32 s36, s12, s35
	s_addc_u32 s37, s13, 0
	s_add_i32 s35, s31, 64
	s_and_b32 s35, s35, 0xff
	s_add_u32 s38, s12, s35
	s_addc_u32 s39, s13, 0
	s_add_i32 s35, s31, 128
	s_and_b32 s35, s35, 0xff
	s_add_u32 s40, s12, s35
	s_addc_u32 s41, s13, 0
	s_add_i32 s35, s31, 192
	s_and_b32 s35, s35, 0xff
	s_add_u32 s42, s12, s35
	s_addc_u32 s43, s13, 0
	global_load_dwordx4 v[104:107], v98, s[36:37]
	global_load_dwordx4 v[108:111], v98, s[38:39]
	global_load_dwordx4 v[112:115], v98, s[40:41]
	global_load_dwordx4 v[116:119], v98, s[42:43]
	global_load_dwordx4 v[120:123], v99, s[36:37]
	global_load_dwordx4 v[124:127], v99, s[38:39]
	global_load_dwordx4 v[128:131], v99, s[40:41]
	global_load_dwordx4 v[132:135], v99, s[42:43]
	global_load_dwordx4 v[136:139], v100, s[36:37]
	global_load_dwordx4 v[140:143], v100, s[38:39]
	global_load_dwordx4 v[144:147], v100, s[40:41]
	global_load_dwordx4 v[148:151], v100, s[42:43]
	global_load_dwordx4 v[152:155], v101, s[36:37]
	global_load_dwordx4 v[156:159], v101, s[38:39]
	global_load_dwordx4 v[160:163], v101, s[40:41]
	global_load_dwordx4 v[164:167], v101, s[42:43]
	s_add_i32 s34, s25, s23
	s_sub_i32 s32, 0x400, s34
	s_ashr_i32 s32, s32, 4
	s_max_i32 s32, s32, 0
	s_min_i32 s32, s32, 6
	s_sub_i32 s33, 0x800, s34
	s_ashr_i32 s33, s33, 4
	s_max_i32 s33, s33, 0
	s_min_i32 s33, s33, 6
	s_cmp_le_u32 s33, 5
	s_cbranch_scc1 .Lepi_v5
	s_waitcnt vmcnt(0)
	s_cmp_lg_u32 s32, 6
	s_cbranch_scc1 .Lepi_r5
	v_mul_f32_e32 v104, 0x3e38aa3b, v104
	v_mul_f32_e32 v105, 0x3e38aa3b, v105
	v_mul_f32_e32 v106, 0x3e38aa3b, v106
	v_mul_f32_e32 v107, 0x3e38aa3b, v107
	v_mul_f32_e32 v108, 0x3e38aa3b, v108
	v_mul_f32_e32 v109, 0x3e38aa3b, v109
	v_mul_f32_e32 v110, 0x3e38aa3b, v110
	v_mul_f32_e32 v111, 0x3e38aa3b, v111
	v_mul_f32_e32 v112, 0x3e38aa3b, v112
	v_mul_f32_e32 v113, 0x3e38aa3b, v113
	v_mul_f32_e32 v114, 0x3e38aa3b, v114
	v_mul_f32_e32 v115, 0x3e38aa3b, v115
	v_mul_f32_e32 v116, 0x3e38aa3b, v116
	v_mul_f32_e32 v117, 0x3e38aa3b, v117
	v_mul_f32_e32 v118, 0x3e38aa3b, v118
	v_mul_f32_e32 v119, 0x3e38aa3b, v119
	v_mul_f32_e32 v120, 0x3e38aa3b, v120
	v_mul_f32_e32 v121, 0x3e38aa3b, v121
	v_mul_f32_e32 v122, 0x3e38aa3b, v122
	v_mul_f32_e32 v123, 0x3e38aa3b, v123
	v_mul_f32_e32 v124, 0x3e38aa3b, v124
	v_mul_f32_e32 v125, 0x3e38aa3b, v125
	v_mul_f32_e32 v126, 0x3e38aa3b, v126
	v_mul_f32_e32 v127, 0x3e38aa3b, v127
	v_mul_f32_e32 v128, 0x3e38aa3b, v128
	v_mul_f32_e32 v129, 0x3e38aa3b, v129
	v_mul_f32_e32 v130, 0x3e38aa3b, v130
	v_mul_f32_e32 v131, 0x3e38aa3b, v131
	v_mul_f32_e32 v132, 0x3e38aa3b, v132
	v_mul_f32_e32 v133, 0x3e38aa3b, v133
	v_mul_f32_e32 v134, 0x3e38aa3b, v134
	v_mul_f32_e32 v135, 0x3e38aa3b, v135
	v_mul_f32_e32 v136, 0x3e38aa3b, v136
	v_mul_f32_e32 v137, 0x3e38aa3b, v137
	v_mul_f32_e32 v138, 0x3e38aa3b, v138
	v_mul_f32_e32 v139, 0x3e38aa3b, v139
	v_mul_f32_e32 v140, 0x3e38aa3b, v140
	v_mul_f32_e32 v141, 0x3e38aa3b, v141
	v_mul_f32_e32 v142, 0x3e38aa3b, v142
	v_mul_f32_e32 v143, 0x3e38aa3b, v143
	v_mul_f32_e32 v144, 0x3e38aa3b, v144
	v_mul_f32_e32 v145, 0x3e38aa3b, v145
	v_mul_f32_e32 v146, 0x3e38aa3b, v146
	v_mul_f32_e32 v147, 0x3e38aa3b, v147
	v_mul_f32_e32 v148, 0x3e38aa3b, v148
	v_mul_f32_e32 v149, 0x3e38aa3b, v149
	v_mul_f32_e32 v150, 0x3e38aa3b, v150
	v_mul_f32_e32 v151, 0x3e38aa3b, v151
	v_mul_f32_e32 v152, 0x3e38aa3b, v152
	v_mul_f32_e32 v153, 0x3e38aa3b, v153
	v_mul_f32_e32 v154, 0x3e38aa3b, v154
	v_mul_f32_e32 v155, 0x3e38aa3b, v155
	v_mul_f32_e32 v156, 0x3e38aa3b, v156
	v_mul_f32_e32 v157, 0x3e38aa3b, v157
	v_mul_f32_e32 v158, 0x3e38aa3b, v158
	v_mul_f32_e32 v159, 0x3e38aa3b, v159
	v_mul_f32_e32 v160, 0x3e38aa3b, v160
	v_mul_f32_e32 v161, 0x3e38aa3b, v161
	v_mul_f32_e32 v162, 0x3e38aa3b, v162
	v_mul_f32_e32 v163, 0x3e38aa3b, v163
	v_mul_f32_e32 v164, 0x3e38aa3b, v164
	v_mul_f32_e32 v165, 0x3e38aa3b, v165
	v_mul_f32_e32 v166, 0x3e38aa3b, v166
	v_mul_f32_e32 v167, 0x3e38aa3b, v167

.LBB2_6:
	s_load_dwordx4 s[0:3], s[0:1], 0x0
	s_add_i32 s9, s22, -8
	s_mov_b32 s28, s23
	s_mov_b32 s29, s20
	v_and_b32_e32 v1, 63, v0
	v_bfe_u32 v3, v0, 4, 2
	v_lshrrev_b32_e32 v2, 2, v1
	v_sub_u32_e32 v3, 0, v3
	v_and_b32_e32 v3, 3, v3
	v_and_b32_e32 v4, 3, v1
	v_xor_b32_e32 v3, v3, v4
	v_lshlrev_b32_e32 v3, 4, v3
	v_lshl_or_b32 v2, v2, 6, v3
	s_lshl_b32 s4, s9, 4
	s_add_i32 s5, s28, s4
	s_lshl_b32 s5, s5, 6
	s_add_i32 s6, s29, s4
	s_lshl_b32 s6, s6, 6
	s_lshl_b32 s8, s9, 10
	s_waitcnt lgkmcnt(0)
	s_add_u32 s10, s0, s5
	s_addc_u32 s11, s1, 0
	s_add_u32 s12, s10, 0x1000
	s_addc_u32 s13, s11, 0
	s_add_u32 s14, s12, 0x1000
	s_addc_u32 s15, s13, 0
	s_add_u32 s16, s2, s6
	s_addc_u32 s17, s3, 0
	s_add_u32 s18, s16, 0x1000
	s_addc_u32 s19, s17, 0
	s_add_u32 s24, s18, 0x1000
	s_addc_u32 s25, s19, 0
	s_add_u32 s26, s24, 0x1000
	s_addc_u32 s27, s25, 0
	v_mov_b32_e32 v5, v2
	v_mov_b32_e32 v6, v2
	s_add_i32 m0, s8, 0
	s_nop 0
	global_load_lds_dwordx4 v5, s[10:11]
	s_add_i32 m0, s8, 4096
	s_nop 0
	global_load_lds_dwordx4 v5, s[12:13]
	s_add_i32 m0, s8, 8192
	s_nop 0
	global_load_lds_dwordx4 v5, s[14:15]
	s_add_i32 m0, s8, 12288
	s_nop 0
	global_load_lds_dwordx4 v6, s[16:17]
	s_add_i32 m0, s8, 16384
	s_nop 0
	global_load_lds_dwordx4 v6, s[18:19]
	s_add_i32 m0, s8, 20480
	s_nop 0
	global_load_lds_dwordx4 v6, s[24:25]
	s_add_i32 m0, s8, 24576
	s_nop 0
	global_load_lds_dwordx4 v6, s[26:27]
	v_add_u32_e32 v5, 196608, v5
	v_add_u32_e32 v6, 262144, v6
	s_add_i32 m0, s8, 28672
	s_nop 0
	global_load_lds_dwordx4 v5, s[10:11]
	s_add_i32 m0, s8, 32768
	s_nop 0
	global_load_lds_dwordx4 v5, s[12:13]
	s_add_i32 m0, s8, 36864
	s_nop 0
	global_load_lds_dwordx4 v5, s[14:15]
	s_add_i32 m0, s8, 40960
	s_nop 0
	global_load_lds_dwordx4 v6, s[16:17]
	s_add_i32 m0, s8, 45056
	s_nop 0
	global_load_lds_dwordx4 v6, s[18:19]
	s_add_i32 m0, s8, 49152
	s_nop 0
	global_load_lds_dwordx4 v6, s[24:25]
	s_add_i32 m0, s8, 53248
	s_nop 0
	global_load_lds_dwordx4 v6, s[26:27]
	v_add_u32_e32 v5, 196608, v5
	v_add_u32_e32 v6, 262144, v6
	s_add_i32 m0, s8, 57344
	s_nop 0
	global_load_lds_dwordx4 v5, s[10:11]
	s_add_i32 m0, s8, 61440
	s_nop 0
	global_load_lds_dwordx4 v5, s[12:13]
	s_add_i32 m0, s8, 65536
	s_nop 0
	global_load_lds_dwordx4 v5, s[14:15]
	s_add_i32 m0, s8, 69632
	s_nop 0
	global_load_lds_dwordx4 v6, s[16:17]
	s_add_i32 m0, s8, 73728
	s_nop 0
	global_load_lds_dwordx4 v6, s[18:19]
	s_add_i32 m0, s8, 77824
	s_nop 0
	global_load_lds_dwordx4 v6, s[24:25]
	s_add_i32 m0, s8, 81920
	s_nop 0
	global_load_lds_dwordx4 v6, s[26:27]
	v_add_u32_e32 v5, 196608, v5
	v_add_u32_e32 v6, 262144, v6
	s_add_i32 m0, s8, 86016
	s_nop 0
	global_load_lds_dwordx4 v5, s[10:11]
	s_add_i32 m0, s8, 90112
	s_nop 0
	global_load_lds_dwordx4 v5, s[12:13]
	s_add_i32 m0, s8, 94208
	s_nop 0
	global_load_lds_dwordx4 v5, s[14:15]
	s_add_i32 m0, s8, 98304
	s_nop 0
	global_load_lds_dwordx4 v6, s[16:17]
	s_add_i32 m0, s8, 102400
	s_nop 0
	global_load_lds_dwordx4 v6, s[18:19]
	s_add_i32 m0, s8, 106496
	s_nop 0
	global_load_lds_dwordx4 v6, s[24:25]
	s_add_i32 m0, s8, 110592
	s_nop 0
	global_load_lds_dwordx4 v6, s[26:27]
	v_add_u32_e32 v5, 196608, v5
	v_add_u32_e32 v6, 262144, v6
	s_waitcnt vmcnt(21)
	s_barrier
	s_mov_b32 s29, 4
	s_mov_b32 s30, 28
.Lg0_ploop:
	s_mul_i32 s28, s29, 28672
	s_add_i32 s28, s28, s8
	s_waitcnt vmcnt(14)
	s_barrier
	s_mov_b32 m0, s28
	s_add_i32 s28, s28, 0x1000
	global_load_lds_dwordx4 v5, s[10:11]
	s_mov_b32 m0, s28
	s_add_i32 s28, s28, 0x1000
	global_load_lds_dwordx4 v5, s[12:13]
	s_mov_b32 m0, s28
	s_add_i32 s28, s28, 0x1000
	global_load_lds_dwordx4 v5, s[14:15]
	s_mov_b32 m0, s28
	s_add_i32 s28, s28, 0x1000
	global_load_lds_dwordx4 v6, s[16:17]
	s_mov_b32 m0, s28
	s_add_i32 s28, s28, 0x1000
	global_load_lds_dwordx4 v6, s[18:19]
	s_mov_b32 m0, s28
	s_add_i32 s28, s28, 0x1000
	global_load_lds_dwordx4 v6, s[24:25]
	s_mov_b32 m0, s28
	s_add_i32 s28, s28, 0x1000
	global_load_lds_dwordx4 v6, s[26:27]
	v_add_u32_e32 v5, 196608, v5
	v_add_u32_e32 v6, 262144, v6
	s_add_i32 s31, s29, 1
	s_cmp_lg_u32 s29, 4
	s_cselect_b32 s29, s31, 0
	s_add_i32 s30, s30, -1
	s_cmp_eq_u32 s30, 0
	s_cbranch_scc0 .Lg0_ploop
	s_waitcnt vmcnt(14)
	s_barrier
	s_waitcnt vmcnt(7)
	s_barrier
	s_waitcnt vmcnt(0)
	s_barrier
	s_waitcnt vmcnt(0)
	s_barrier
	s_endpgm
